# IN bf16 / GATE / IN fp8 epilogues: second half's row-factor loads issued with the first half's (no store drain), counted waits at first use; on top of UP epilogue de-serialisation
# speedup vs baseline: 1.0078x; 1.0019x over previous
.LBB0_178:
	v_lshl_add_u32 v8, s20, 8, v194
	v_ashrrev_i32_e32 v9, 31, v8
	s_nop 15
	s_nop 15
	v_lshl_add_u64 v[10:11], v[8:9], 2, s[4:5]
	global_load_dword v22, v[10:11], off
	v_or_b32_e32 v16, 16, v8
	v_ashrrev_i32_e32 v17, 31, v16
	v_lshl_add_u64 v[6:7], v[16:17], 2, s[4:5]
	global_load_dword v21, v[6:7], off
	v_or_b32_e32 v14, 32, v8
	v_ashrrev_i32_e32 v15, 31, v14
	v_or_b32_e32 v12, 48, v8
	v_lshl_add_u64 v[6:7], v[14:15], 2, s[4:5]
	v_ashrrev_i32_e32 v13, 31, v12
	global_load_dword v20, v[6:7], off
	v_lshl_add_u64 v[6:7], v[12:13], 2, s[4:5]
	v_lshl_or_b32 v4, s21, 8, v211
	global_load_dword v9, v[6:7], off
	global_load_dword v226, v[10:11], off offset:512
	global_load_dword v229, v[10:11], off offset:576
	global_load_dword v240, v[10:11], off offset:640
	global_load_dword v251, v[10:11], off offset:704
	v_mov_b64_e32 v[6:7], s[8:9]
	s_movk_i32 s13, 0x7200
	v_ashrrev_i32_e32 v5, 31, v4
	v_mad_i64_i32 v[18:19], s[20:21], v8, s13, v[6:7]
	v_lshl_add_u64 v[18:19], v[18:19], 0, v[4:5]
	s_andn2_b64 vcc, exec, s[36:37]
	s_waitcnt lgkmcnt(0)
	s_waitcnt vmcnt(7)
	v_mul_f32_e32 v13, 0x3c000000, v22
	v_mul_f32_e32 v13, 0xbfb8aa3b, v13
	v_mul_f32_e32 v15, v160, v13
	v_mul_f32_e32 v17, v156, v13
	v_exp_f32_e32 v15, v15
	v_exp_f32_e32 v17, v17
	v_mul_f32_e32 v22, v161, v13
	v_mul_f32_e32 v23, v157, v13
	v_exp_f32_e32 v22, v22
	v_exp_f32_e32 v23, v23
	v_fmamk_f32 v15, v15, 0x3b808081, v227
	v_fmamk_f32 v17, v17, 0x3b808081, v227
	v_rcp_f32_e32 v15, v15
	v_rcp_f32_e32 v17, v17
	v_fmamk_f32 v22, v22, 0x3b808081, v227
	v_fmamk_f32 v23, v23, 0x3b808081, v227
	v_rcp_f32_e32 v22, v22
	v_rcp_f32_e32 v23, v23
	v_max_f32_e32 v15, 1.0, v15
	v_max_f32_e32 v17, 1.0, v17
	v_cvt_pk_u8_f32 v15, v15, 0, 0
	v_cvt_pk_u8_f32 v17, v17, 0, 0
	v_max_f32_e32 v22, 1.0, v22
	v_max_f32_e32 v23, 1.0, v23
	v_cvt_pk_u8_f32 v15, v22, 1, v15
	v_cvt_pk_u8_f32 v17, v23, 1, v17
	v_mul_f32_e32 v22, v162, v13
	v_mul_f32_e32 v23, v158, v13
	v_exp_f32_e32 v22, v22
	v_exp_f32_e32 v23, v23
	s_waitcnt vmcnt(4)
	v_mul_f32_e32 v9, 0x3c000000, v9
	v_mul_f32_e32 v9, 0xbfb8aa3b, v9
	v_fmamk_f32 v22, v22, 0x3b808081, v227
	v_fmamk_f32 v23, v23, 0x3b808081, v227
	v_rcp_f32_e32 v22, v22
	v_rcp_f32_e32 v23, v23
	v_max_f32_e32 v22, 1.0, v22
	v_max_f32_e32 v23, 1.0, v23
	v_cvt_pk_u8_f32 v15, v22, 2, v15
	v_cvt_pk_u8_f32 v17, v23, 2, v17
	v_mul_f32_e32 v22, v163, v13
	v_mul_f32_e32 v23, v159, v13
	v_exp_f32_e32 v22, v22
	v_exp_f32_e32 v23, v23
	v_fmamk_f32 v22, v22, 0x3b808081, v227
	v_fmamk_f32 v23, v23, 0x3b808081, v227
	v_rcp_f32_e32 v22, v22
	v_rcp_f32_e32 v23, v23
	v_max_f32_e32 v22, 1.0, v22
	v_max_f32_e32 v23, 1.0, v23
	v_cvt_pk_u8_f32 v22, v22, 3, v15
	v_cvt_pk_u8_f32 v23, v23, 3, v17
	v_mul_f32_e32 v15, v152, v13
	global_store_dwordx2 v[18:19], v[22:23], off
	v_exp_f32_e32 v15, v15
	v_mul_f32_e32 v22, v153, v13
	v_exp_f32_e32 v22, v22
	v_mul_f32_e32 v17, v148, v13
	v_fmamk_f32 v15, v15, 0x3b808081, v227
	v_rcp_f32_e32 v15, v15
	v_fmamk_f32 v22, v22, 0x3b808081, v227
	v_rcp_f32_e32 v22, v22
	v_exp_f32_e32 v17, v17
	v_max_f32_e32 v15, 1.0, v15
	v_cvt_pk_u8_f32 v15, v15, 0, 0
	v_max_f32_e32 v22, 1.0, v22
	v_mul_f32_e32 v23, v149, v13
	v_exp_f32_e32 v23, v23
	v_cvt_pk_u8_f32 v15, v22, 1, v15
	v_mul_f32_e32 v22, v154, v13
	v_exp_f32_e32 v22, v22
	v_fmamk_f32 v17, v17, 0x3b808081, v227
	v_rcp_f32_e32 v17, v17
	v_fmamk_f32 v23, v23, 0x3b808081, v227
	v_rcp_f32_e32 v23, v23
	v_fmamk_f32 v22, v22, 0x3b808081, v227
	v_rcp_f32_e32 v22, v22
	v_max_f32_e32 v17, 1.0, v17
	v_cvt_pk_u8_f32 v17, v17, 0, 0
	v_max_f32_e32 v23, 1.0, v23
	v_cvt_pk_u8_f32 v17, v23, 1, v17
	v_max_f32_e32 v22, 1.0, v22
	v_mul_f32_e32 v23, v150, v13
	v_exp_f32_e32 v23, v23
	v_cvt_pk_u8_f32 v15, v22, 2, v15
	v_mul_f32_e32 v22, v155, v13
	v_mul_f32_e32 v13, v151, v13
	v_exp_f32_e32 v13, v13
	v_exp_f32_e32 v22, v22
	v_fmamk_f32 v23, v23, 0x3b808081, v227
	v_rcp_f32_e32 v23, v23
	v_fmamk_f32 v13, v13, 0x3b808081, v227
	v_fmamk_f32 v22, v22, 0x3b808081, v227
	v_rcp_f32_e32 v13, v13
	v_rcp_f32_e32 v22, v22
	v_max_f32_e32 v23, 1.0, v23
	v_cvt_pk_u8_f32 v17, v23, 2, v17
	v_max_f32_e32 v13, 1.0, v13
	v_max_f32_e32 v22, 1.0, v22
	v_cvt_pk_u8_f32 v23, v13, 3, v17
	v_mul_f32_e32 v13, 0x3c000000, v21
	v_cvt_pk_u8_f32 v22, v22, 3, v15
	v_mul_f32_e32 v13, 0xbfb8aa3b, v13
	global_store_dwordx2 v[18:19], v[22:23], off offset:128
	v_mul_f32_e32 v15, v144, v13
	v_mul_f32_e32 v18, v140, v13
	v_exp_f32_e32 v15, v15
	v_exp_f32_e32 v18, v18
	v_mul_f32_e32 v19, v145, v13
	v_mul_f32_e32 v21, v141, v13
	v_exp_f32_e32 v19, v19
	v_exp_f32_e32 v21, v21
	v_fmamk_f32 v15, v15, 0x3b808081, v227
	v_fmamk_f32 v18, v18, 0x3b808081, v227
	v_rcp_f32_e32 v15, v15
	v_rcp_f32_e32 v18, v18
	v_fmamk_f32 v19, v19, 0x3b808081, v227
	v_fmamk_f32 v21, v21, 0x3b808081, v227
	v_rcp_f32_e32 v19, v19
	v_rcp_f32_e32 v21, v21
	v_max_f32_e32 v15, 1.0, v15
	v_max_f32_e32 v18, 1.0, v18
	v_cvt_pk_u8_f32 v15, v15, 0, 0
	v_cvt_pk_u8_f32 v18, v18, 0, 0
	v_max_f32_e32 v19, 1.0, v19
	v_max_f32_e32 v21, 1.0, v21
	v_cvt_pk_u8_f32 v15, v19, 1, v15
	v_cvt_pk_u8_f32 v18, v21, 1, v18
	v_mul_f32_e32 v19, v146, v13
	v_mul_f32_e32 v21, v142, v13
	v_exp_f32_e32 v19, v19
	v_exp_f32_e32 v21, v21
	v_mad_i64_i32 v[16:17], s[20:21], v16, s13, v[6:7]
	v_fmamk_f32 v19, v19, 0x3b808081, v227
	v_fmamk_f32 v21, v21, 0x3b808081, v227
	v_rcp_f32_e32 v19, v19
	v_rcp_f32_e32 v21, v21
	v_lshl_add_u64 v[16:17], v[16:17], 0, v[4:5]
	v_max_f32_e32 v19, 1.0, v19
	v_max_f32_e32 v21, 1.0, v21
	v_cvt_pk_u8_f32 v15, v19, 2, v15
	v_cvt_pk_u8_f32 v19, v21, 2, v18
	v_mul_f32_e32 v18, v147, v13
	v_mul_f32_e32 v21, v143, v13
	v_exp_f32_e32 v18, v18
	v_exp_f32_e32 v21, v21
	v_fmamk_f32 v18, v18, 0x3b808081, v227
	v_fmamk_f32 v21, v21, 0x3b808081, v227
	v_rcp_f32_e32 v18, v18
	v_rcp_f32_e32 v21, v21
	v_max_f32_e32 v18, 1.0, v18
	v_max_f32_e32 v21, 1.0, v21
	v_cvt_pk_u8_f32 v18, v18, 3, v15
	v_cvt_pk_u8_f32 v19, v21, 3, v19
	global_store_dwordx2 v[16:17], v[18:19], off
	v_mul_f32_e32 v15, v136, v13
	v_mul_f32_e32 v18, v132, v13
	v_exp_f32_e32 v15, v15
	v_exp_f32_e32 v18, v18
	v_mul_f32_e32 v19, v137, v13
	v_mul_f32_e32 v21, v133, v13
	v_exp_f32_e32 v19, v19
	v_exp_f32_e32 v21, v21
	v_fmamk_f32 v15, v15, 0x3b808081, v227
	v_fmamk_f32 v18, v18, 0x3b808081, v227
	v_rcp_f32_e32 v15, v15
	v_rcp_f32_e32 v18, v18
	v_fmamk_f32 v19, v19, 0x3b808081, v227
	v_fmamk_f32 v21, v21, 0x3b808081, v227
	v_rcp_f32_e32 v19, v19
	v_rcp_f32_e32 v21, v21
	v_max_f32_e32 v15, 1.0, v15
	v_max_f32_e32 v18, 1.0, v18
	v_cvt_pk_u8_f32 v15, v15, 0, 0
	v_cvt_pk_u8_f32 v18, v18, 0, 0
	v_max_f32_e32 v19, 1.0, v19
	v_max_f32_e32 v21, 1.0, v21
	v_cvt_pk_u8_f32 v15, v19, 1, v15
	v_cvt_pk_u8_f32 v18, v21, 1, v18
	v_mul_f32_e32 v19, v138, v13
	v_mul_f32_e32 v21, v134, v13
	v_exp_f32_e32 v19, v19
	v_exp_f32_e32 v21, v21
	v_fmamk_f32 v19, v19, 0x3b808081, v227
	v_fmamk_f32 v21, v21, 0x3b808081, v227
	v_rcp_f32_e32 v19, v19
	v_rcp_f32_e32 v21, v21
	v_max_f32_e32 v19, 1.0, v19
	v_max_f32_e32 v21, 1.0, v21
	v_cvt_pk_u8_f32 v15, v19, 2, v15
	v_cvt_pk_u8_f32 v19, v21, 2, v18
	v_mul_f32_e32 v18, v139, v13
	v_mul_f32_e32 v13, v135, v13
	v_exp_f32_e32 v13, v13
	v_exp_f32_e32 v18, v18
	v_fmamk_f32 v13, v13, 0x3b808081, v227
	v_fmamk_f32 v18, v18, 0x3b808081, v227
	v_rcp_f32_e32 v13, v13
	v_rcp_f32_e32 v18, v18
	v_max_f32_e32 v13, 1.0, v13
	v_max_f32_e32 v18, 1.0, v18
	v_cvt_pk_u8_f32 v19, v13, 3, v19
	v_mul_f32_e32 v13, 0x3c000000, v20
	v_cvt_pk_u8_f32 v18, v18, 3, v15
	v_mul_f32_e32 v13, 0xbfb8aa3b, v13
	global_store_dwordx2 v[16:17], v[18:19], off offset:128
	v_mul_f32_e32 v16, v128, v13
	v_mul_f32_e32 v17, v124, v13
	v_exp_f32_e32 v16, v16
	v_exp_f32_e32 v17, v17
	v_mul_f32_e32 v18, v129, v13
	v_mul_f32_e32 v19, v125, v13
	v_exp_f32_e32 v18, v18
	v_exp_f32_e32 v19, v19
	v_fmamk_f32 v16, v16, 0x3b808081, v227
	v_fmamk_f32 v17, v17, 0x3b808081, v227
	v_rcp_f32_e32 v16, v16
	v_rcp_f32_e32 v17, v17
	v_fmamk_f32 v18, v18, 0x3b808081, v227
	v_fmamk_f32 v19, v19, 0x3b808081, v227
	v_rcp_f32_e32 v18, v18
	v_rcp_f32_e32 v19, v19
	v_max_f32_e32 v16, 1.0, v16
	v_max_f32_e32 v17, 1.0, v17
	v_cvt_pk_u8_f32 v16, v16, 0, 0
	v_cvt_pk_u8_f32 v17, v17, 0, 0
	v_max_f32_e32 v18, 1.0, v18
	v_max_f32_e32 v19, 1.0, v19
	v_cvt_pk_u8_f32 v16, v18, 1, v16
	v_cvt_pk_u8_f32 v17, v19, 1, v17
	v_mul_f32_e32 v18, v130, v13
	v_mul_f32_e32 v19, v126, v13
	v_exp_f32_e32 v18, v18
	v_exp_f32_e32 v19, v19
	v_mad_i64_i32 v[14:15], s[20:21], v14, s13, v[6:7]
	v_fmamk_f32 v18, v18, 0x3b808081, v227
	v_fmamk_f32 v19, v19, 0x3b808081, v227
	v_rcp_f32_e32 v18, v18
	v_rcp_f32_e32 v19, v19
	v_lshl_add_u64 v[14:15], v[14:15], 0, v[4:5]
	v_max_f32_e32 v18, 1.0, v18
	v_max_f32_e32 v19, 1.0, v19
	v_cvt_pk_u8_f32 v16, v18, 2, v16
	v_cvt_pk_u8_f32 v17, v19, 2, v17
	v_mul_f32_e32 v18, v131, v13
	v_mul_f32_e32 v19, v127, v13
	v_exp_f32_e32 v18, v18
	v_exp_f32_e32 v19, v19
	v_fmamk_f32 v18, v18, 0x3b808081, v227
	v_fmamk_f32 v19, v19, 0x3b808081, v227
	v_rcp_f32_e32 v18, v18
	v_rcp_f32_e32 v19, v19
	v_max_f32_e32 v18, 1.0, v18
	v_max_f32_e32 v19, 1.0, v19
	v_cvt_pk_u8_f32 v16, v18, 3, v16
	v_cvt_pk_u8_f32 v17, v19, 3, v17
	global_store_dwordx2 v[14:15], v[16:17], off
	v_mul_f32_e32 v16, v120, v13
	v_exp_f32_e32 v16, v16
	v_mul_f32_e32 v18, v121, v13
	v_exp_f32_e32 v18, v18
	v_mul_f32_e32 v17, v116, v13
	v_fmamk_f32 v16, v16, 0x3b808081, v227
	v_rcp_f32_e32 v16, v16
	v_fmamk_f32 v18, v18, 0x3b808081, v227
	v_rcp_f32_e32 v18, v18
	v_exp_f32_e32 v17, v17
	v_max_f32_e32 v16, 1.0, v16
	v_cvt_pk_u8_f32 v16, v16, 0, 0
	v_max_f32_e32 v18, 1.0, v18
	v_mul_f32_e32 v19, v117, v13
	v_exp_f32_e32 v19, v19
	v_cvt_pk_u8_f32 v16, v18, 1, v16
	v_mul_f32_e32 v18, v122, v13
	v_exp_f32_e32 v18, v18
	v_fmamk_f32 v17, v17, 0x3b808081, v227
	v_rcp_f32_e32 v17, v17
	v_fmamk_f32 v19, v19, 0x3b808081, v227
	v_rcp_f32_e32 v19, v19
	v_fmamk_f32 v18, v18, 0x3b808081, v227
	v_rcp_f32_e32 v18, v18
	v_max_f32_e32 v17, 1.0, v17
	v_cvt_pk_u8_f32 v17, v17, 0, 0
	v_max_f32_e32 v19, 1.0, v19
	v_cvt_pk_u8_f32 v17, v19, 1, v17
	v_max_f32_e32 v18, 1.0, v18
	v_mul_f32_e32 v19, v118, v13
	v_exp_f32_e32 v19, v19
	v_cvt_pk_u8_f32 v16, v18, 2, v16
	v_mul_f32_e32 v18, v123, v13
	v_mul_f32_e32 v13, v119, v13
	v_exp_f32_e32 v18, v18
	v_exp_f32_e32 v13, v13
	v_fmamk_f32 v19, v19, 0x3b808081, v227
	v_rcp_f32_e32 v19, v19
	v_fmamk_f32 v18, v18, 0x3b808081, v227
	v_fmamk_f32 v13, v13, 0x3b808081, v227
	v_rcp_f32_e32 v18, v18
	v_rcp_f32_e32 v13, v13
	v_max_f32_e32 v19, 1.0, v19
	v_cvt_pk_u8_f32 v17, v19, 2, v17
	v_max_f32_e32 v18, 1.0, v18
	v_max_f32_e32 v13, 1.0, v13
	v_cvt_pk_u8_f32 v16, v18, 3, v16
	v_cvt_pk_u8_f32 v17, v13, 3, v17
	global_store_dwordx2 v[14:15], v[16:17], off offset:128
	v_mul_f32_e32 v14, v112, v9
	v_mul_f32_e32 v15, v108, v9
	v_exp_f32_e32 v14, v14
	v_exp_f32_e32 v15, v15
	v_mul_f32_e32 v16, v113, v9
	v_mul_f32_e32 v17, v109, v9
	v_exp_f32_e32 v16, v16
	v_exp_f32_e32 v17, v17
	v_fmamk_f32 v14, v14, 0x3b808081, v227
	v_fmamk_f32 v15, v15, 0x3b808081, v227
	v_rcp_f32_e32 v14, v14
	v_rcp_f32_e32 v15, v15
	v_fmamk_f32 v16, v16, 0x3b808081, v227
	v_fmamk_f32 v17, v17, 0x3b808081, v227
	v_rcp_f32_e32 v16, v16
	v_rcp_f32_e32 v17, v17
	v_max_f32_e32 v14, 1.0, v14
	v_max_f32_e32 v15, 1.0, v15
	v_cvt_pk_u8_f32 v14, v14, 0, 0
	v_cvt_pk_u8_f32 v15, v15, 0, 0
	v_max_f32_e32 v16, 1.0, v16
	v_max_f32_e32 v17, 1.0, v17
	v_cvt_pk_u8_f32 v14, v16, 1, v14
	v_cvt_pk_u8_f32 v15, v17, 1, v15
	v_mul_f32_e32 v16, v114, v9
	v_mul_f32_e32 v17, v110, v9
	v_exp_f32_e32 v16, v16
	v_exp_f32_e32 v17, v17
	v_mad_i64_i32 v[12:13], s[20:21], v12, s13, v[6:7]
	v_fmamk_f32 v16, v16, 0x3b808081, v227
	v_fmamk_f32 v17, v17, 0x3b808081, v227
	v_rcp_f32_e32 v16, v16
	v_rcp_f32_e32 v17, v17
	v_lshl_add_u64 v[12:13], v[12:13], 0, v[4:5]
	v_add_u32_e32 v18, 0x90, v8
	v_max_f32_e32 v16, 1.0, v16
	v_max_f32_e32 v17, 1.0, v17
	v_cvt_pk_u8_f32 v14, v16, 2, v14
	v_cvt_pk_u8_f32 v15, v17, 2, v15
	v_mul_f32_e32 v16, v115, v9
	v_mul_f32_e32 v17, v111, v9
	v_exp_f32_e32 v16, v16
	v_exp_f32_e32 v17, v17
	v_fmamk_f32 v16, v16, 0x3b808081, v227
	v_fmamk_f32 v17, v17, 0x3b808081, v227
	v_rcp_f32_e32 v16, v16
	v_rcp_f32_e32 v17, v17
	v_max_f32_e32 v16, 1.0, v16
	v_max_f32_e32 v17, 1.0, v17
	v_cvt_pk_u8_f32 v14, v16, 3, v14
	v_cvt_pk_u8_f32 v15, v17, 3, v15
	global_store_dwordx2 v[12:13], v[14:15], off
	v_mul_f32_e32 v14, v104, v9
	v_exp_f32_e32 v14, v14
	v_mul_f32_e32 v16, v105, v9
	v_exp_f32_e32 v16, v16
	v_mul_f32_e32 v15, v100, v9
	v_fmamk_f32 v14, v14, 0x3b808081, v227
	v_rcp_f32_e32 v14, v14
	v_fmamk_f32 v16, v16, 0x3b808081, v227
	v_rcp_f32_e32 v16, v16
	v_exp_f32_e32 v15, v15
	v_max_f32_e32 v14, 1.0, v14
	v_cvt_pk_u8_f32 v14, v14, 0, 0
	v_max_f32_e32 v16, 1.0, v16
	v_mul_f32_e32 v17, v101, v9
	v_exp_f32_e32 v17, v17
	v_cvt_pk_u8_f32 v14, v16, 1, v14
	v_mul_f32_e32 v16, v106, v9
	v_exp_f32_e32 v16, v16
	v_fmamk_f32 v15, v15, 0x3b808081, v227
	v_rcp_f32_e32 v15, v15
	v_fmamk_f32 v17, v17, 0x3b808081, v227
	v_rcp_f32_e32 v17, v17
	v_fmamk_f32 v16, v16, 0x3b808081, v227
	v_rcp_f32_e32 v16, v16
	v_max_f32_e32 v15, 1.0, v15
	v_cvt_pk_u8_f32 v15, v15, 0, 0
	v_max_f32_e32 v17, 1.0, v17
	v_cvt_pk_u8_f32 v15, v17, 1, v15
	v_max_f32_e32 v16, 1.0, v16
	v_mul_f32_e32 v17, v102, v9
	v_exp_f32_e32 v17, v17
	v_cvt_pk_u8_f32 v14, v16, 2, v14
	v_mul_f32_e32 v16, v107, v9
	v_mul_f32_e32 v9, v103, v9
	v_exp_f32_e32 v16, v16
	v_exp_f32_e32 v9, v9
	v_fmamk_f32 v17, v17, 0x3b808081, v227
	v_rcp_f32_e32 v17, v17
	v_fmamk_f32 v16, v16, 0x3b808081, v227
	v_fmamk_f32 v9, v9, 0x3b808081, v227
	v_rcp_f32_e32 v16, v16
	v_rcp_f32_e32 v9, v9
	v_max_f32_e32 v17, 1.0, v17
	v_cvt_pk_u8_f32 v15, v17, 2, v15
	v_max_f32_e32 v16, 1.0, v16
	v_max_f32_e32 v9, 1.0, v9
	v_cvt_pk_u8_f32 v14, v16, 3, v14
	v_cvt_pk_u8_f32 v15, v9, 3, v15
	global_store_dwordx2 v[12:13], v[14:15], off offset:128
	s_nop 1
	s_waitcnt vmcnt(11)
	v_mov_b32_e32 v15, v226
	v_add_u32_e32 v9, 0x80, v8
	s_waitcnt vmcnt(10)
	v_mov_b32_e32 v19, v229
	s_waitcnt vmcnt(9)
	v_mov_b32_e32 v13, v240
	v_add_u32_e32 v14, 0xa0, v8
	s_waitcnt vmcnt(8)
	v_mov_b32_e32 v10, v251
	v_add_u32_e32 v12, 0xb0, v8
	v_mad_i64_i32 v[8:9], s[20:21], v9, s13, v[6:7]
	v_lshl_add_u64 v[8:9], v[8:9], 0, v[4:5]
	s_waitcnt lgkmcnt(0)
	v_mul_f32_e32 v11, 0x3c000000, v15
	v_mul_f32_e32 v11, 0xbfb8aa3b, v11
	v_mul_f32_e32 v15, v96, v11
	v_mul_f32_e32 v16, v92, v11
	v_exp_f32_e32 v15, v15
	v_exp_f32_e32 v16, v16
	v_mul_f32_e32 v17, v97, v11
	v_mul_f32_e32 v20, v93, v11
	v_exp_f32_e32 v17, v17
	v_exp_f32_e32 v20, v20
	v_fmamk_f32 v15, v15, 0x3b808081, v227
	v_fmamk_f32 v16, v16, 0x3b808081, v227
	v_rcp_f32_e32 v15, v15
	v_rcp_f32_e32 v16, v16
	v_fmamk_f32 v17, v17, 0x3b808081, v227
	v_fmamk_f32 v20, v20, 0x3b808081, v227
	v_rcp_f32_e32 v17, v17
	v_rcp_f32_e32 v20, v20
	v_max_f32_e32 v15, 1.0, v15
	v_max_f32_e32 v16, 1.0, v16
	v_cvt_pk_u8_f32 v15, v15, 0, 0
	v_cvt_pk_u8_f32 v16, v16, 0, 0
	v_max_f32_e32 v17, 1.0, v17
	v_max_f32_e32 v20, 1.0, v20
	v_cvt_pk_u8_f32 v15, v17, 1, v15
	v_cvt_pk_u8_f32 v16, v20, 1, v16
	v_mul_f32_e32 v17, v98, v11
	v_mul_f32_e32 v20, v94, v11
	v_exp_f32_e32 v17, v17
	v_exp_f32_e32 v20, v20
	v_fmamk_f32 v17, v17, 0x3b808081, v227
	v_fmamk_f32 v20, v20, 0x3b808081, v227
	v_rcp_f32_e32 v17, v17
	v_rcp_f32_e32 v20, v20
	v_max_f32_e32 v17, 1.0, v17
	v_max_f32_e32 v20, 1.0, v20
	v_cvt_pk_u8_f32 v15, v17, 2, v15
	v_cvt_pk_u8_f32 v17, v20, 2, v16
	v_mul_f32_e32 v16, v99, v11
	v_mul_f32_e32 v20, v95, v11
	v_exp_f32_e32 v16, v16
	v_exp_f32_e32 v20, v20
	v_fmamk_f32 v16, v16, 0x3b808081, v227
	v_fmamk_f32 v20, v20, 0x3b808081, v227
	v_rcp_f32_e32 v16, v16
	v_rcp_f32_e32 v20, v20
	v_max_f32_e32 v16, 1.0, v16
	v_max_f32_e32 v20, 1.0, v20
	v_cvt_pk_u8_f32 v16, v16, 3, v15
	v_cvt_pk_u8_f32 v17, v20, 3, v17
	global_store_dwordx2 v[8:9], v[16:17], off
	v_mul_f32_e32 v15, v88, v11
	v_mul_f32_e32 v16, v84, v11
	v_exp_f32_e32 v15, v15
	v_exp_f32_e32 v16, v16
	v_mul_f32_e32 v17, v89, v11
	v_mul_f32_e32 v20, v85, v11
	v_exp_f32_e32 v17, v17
	v_exp_f32_e32 v20, v20
	v_fmamk_f32 v15, v15, 0x3b808081, v227
	v_fmamk_f32 v16, v16, 0x3b808081, v227
	v_rcp_f32_e32 v15, v15
	v_rcp_f32_e32 v16, v16
	v_fmamk_f32 v17, v17, 0x3b808081, v227
	v_fmamk_f32 v20, v20, 0x3b808081, v227
	v_rcp_f32_e32 v17, v17
	v_rcp_f32_e32 v20, v20
	v_max_f32_e32 v15, 1.0, v15
	v_max_f32_e32 v16, 1.0, v16
	v_cvt_pk_u8_f32 v15, v15, 0, 0
	v_cvt_pk_u8_f32 v16, v16, 0, 0
	v_max_f32_e32 v17, 1.0, v17
	v_max_f32_e32 v20, 1.0, v20
	v_cvt_pk_u8_f32 v15, v17, 1, v15
	v_cvt_pk_u8_f32 v16, v20, 1, v16
	v_mul_f32_e32 v17, v90, v11
	v_mul_f32_e32 v20, v86, v11
	v_exp_f32_e32 v17, v17
	v_exp_f32_e32 v20, v20
	v_fmamk_f32 v17, v17, 0x3b808081, v227
	v_fmamk_f32 v20, v20, 0x3b808081, v227
	v_rcp_f32_e32 v17, v17
	v_rcp_f32_e32 v20, v20
	v_max_f32_e32 v17, 1.0, v17
	v_max_f32_e32 v20, 1.0, v20
	v_cvt_pk_u8_f32 v15, v17, 2, v15
	v_cvt_pk_u8_f32 v17, v20, 2, v16
	v_mul_f32_e32 v16, v91, v11
	v_mul_f32_e32 v11, v87, v11
	v_exp_f32_e32 v11, v11
	v_exp_f32_e32 v16, v16
	v_fmamk_f32 v11, v11, 0x3b808081, v227
	v_fmamk_f32 v16, v16, 0x3b808081, v227
	v_rcp_f32_e32 v11, v11
	v_rcp_f32_e32 v16, v16
	v_max_f32_e32 v11, 1.0, v11
	v_max_f32_e32 v16, 1.0, v16
	v_cvt_pk_u8_f32 v17, v11, 3, v17
	v_mul_f32_e32 v11, 0x3c000000, v19
	v_cvt_pk_u8_f32 v16, v16, 3, v15
	v_mul_f32_e32 v11, 0xbfb8aa3b, v11
	global_store_dwordx2 v[8:9], v[16:17], off offset:128
	v_mul_f32_e32 v15, v80, v11
	v_mul_f32_e32 v16, v76, v11
	v_mad_i64_i32 v[8:9], s[20:21], v18, s13, v[6:7]
	v_exp_f32_e32 v15, v15
	v_exp_f32_e32 v16, v16
	v_mul_f32_e32 v17, v81, v11
	v_mul_f32_e32 v18, v77, v11
	v_exp_f32_e32 v17, v17
	v_exp_f32_e32 v18, v18
	v_fmamk_f32 v15, v15, 0x3b808081, v227
	v_fmamk_f32 v16, v16, 0x3b808081, v227
	v_rcp_f32_e32 v15, v15
	v_rcp_f32_e32 v16, v16
	v_fmamk_f32 v17, v17, 0x3b808081, v227
	v_fmamk_f32 v18, v18, 0x3b808081, v227
	v_rcp_f32_e32 v17, v17
	v_rcp_f32_e32 v18, v18
	v_max_f32_e32 v15, 1.0, v15
	v_max_f32_e32 v16, 1.0, v16
	v_cvt_pk_u8_f32 v15, v15, 0, 0
	v_cvt_pk_u8_f32 v16, v16, 0, 0
	v_max_f32_e32 v17, 1.0, v17
	v_max_f32_e32 v18, 1.0, v18
	v_cvt_pk_u8_f32 v15, v17, 1, v15
	v_cvt_pk_u8_f32 v16, v18, 1, v16
	v_mul_f32_e32 v17, v82, v11
	v_mul_f32_e32 v18, v78, v11
	v_exp_f32_e32 v17, v17
	v_exp_f32_e32 v18, v18
	v_lshl_add_u64 v[8:9], v[8:9], 0, v[4:5]
	v_fmamk_f32 v17, v17, 0x3b808081, v227
	v_fmamk_f32 v18, v18, 0x3b808081, v227
	v_rcp_f32_e32 v17, v17
	v_rcp_f32_e32 v18, v18
	v_max_f32_e32 v17, 1.0, v17
	v_max_f32_e32 v18, 1.0, v18
	v_cvt_pk_u8_f32 v15, v17, 2, v15
	v_cvt_pk_u8_f32 v17, v18, 2, v16
	v_mul_f32_e32 v16, v83, v11
	v_mul_f32_e32 v18, v79, v11
	v_exp_f32_e32 v16, v16
	v_exp_f32_e32 v18, v18
	v_fmamk_f32 v16, v16, 0x3b808081, v227
	v_fmamk_f32 v18, v18, 0x3b808081, v227
	v_rcp_f32_e32 v16, v16
	v_rcp_f32_e32 v18, v18
	v_max_f32_e32 v16, 1.0, v16
	v_max_f32_e32 v18, 1.0, v18
	v_cvt_pk_u8_f32 v16, v16, 3, v15
	v_cvt_pk_u8_f32 v17, v18, 3, v17
	global_store_dwordx2 v[8:9], v[16:17], off
	v_mul_f32_e32 v15, v72, v11
	v_mul_f32_e32 v16, v68, v11
	v_exp_f32_e32 v15, v15
	v_exp_f32_e32 v16, v16
	v_mul_f32_e32 v17, v73, v11
	v_mul_f32_e32 v18, v69, v11
	v_exp_f32_e32 v17, v17
	v_exp_f32_e32 v18, v18
	v_fmamk_f32 v15, v15, 0x3b808081, v227
	v_fmamk_f32 v16, v16, 0x3b808081, v227
	v_rcp_f32_e32 v15, v15
	v_rcp_f32_e32 v16, v16
	v_fmamk_f32 v17, v17, 0x3b808081, v227
	v_fmamk_f32 v18, v18, 0x3b808081, v227
	v_rcp_f32_e32 v17, v17
	v_rcp_f32_e32 v18, v18
	v_max_f32_e32 v15, 1.0, v15
	v_max_f32_e32 v16, 1.0, v16
	v_cvt_pk_u8_f32 v15, v15, 0, 0
	v_cvt_pk_u8_f32 v16, v16, 0, 0
	v_max_f32_e32 v17, 1.0, v17
	v_max_f32_e32 v18, 1.0, v18
	v_cvt_pk_u8_f32 v15, v17, 1, v15
	v_cvt_pk_u8_f32 v16, v18, 1, v16
	v_mul_f32_e32 v17, v74, v11
	v_mul_f32_e32 v18, v70, v11
	v_exp_f32_e32 v17, v17
	v_exp_f32_e32 v18, v18
	v_fmamk_f32 v17, v17, 0x3b808081, v227
	v_fmamk_f32 v18, v18, 0x3b808081, v227
	v_rcp_f32_e32 v17, v17
	v_rcp_f32_e32 v18, v18
	v_max_f32_e32 v17, 1.0, v17
	v_max_f32_e32 v18, 1.0, v18
	v_cvt_pk_u8_f32 v15, v17, 2, v15
	v_cvt_pk_u8_f32 v17, v18, 2, v16
	v_mul_f32_e32 v16, v75, v11
	v_mul_f32_e32 v11, v71, v11
	v_exp_f32_e32 v11, v11
	v_exp_f32_e32 v16, v16
	v_fmamk_f32 v11, v11, 0x3b808081, v227
	v_fmamk_f32 v16, v16, 0x3b808081, v227
	v_rcp_f32_e32 v11, v11
	v_rcp_f32_e32 v16, v16
	v_max_f32_e32 v11, 1.0, v11
	v_max_f32_e32 v16, 1.0, v16
	v_cvt_pk_u8_f32 v17, v11, 3, v17
	v_mul_f32_e32 v11, 0x3c000000, v13
	v_cvt_pk_u8_f32 v16, v16, 3, v15
	v_mul_f32_e32 v11, 0xbfb8aa3b, v11
	global_store_dwordx2 v[8:9], v[16:17], off offset:128
	v_mad_i64_i32 v[8:9], s[20:21], v14, s13, v[6:7]
	v_mul_f32_e32 v13, v64, v11
	v_mul_f32_e32 v14, v60, v11
	v_exp_f32_e32 v13, v13
	v_exp_f32_e32 v14, v14
	v_mul_f32_e32 v15, v65, v11
	v_mul_f32_e32 v16, v61, v11
	v_exp_f32_e32 v15, v15
	v_exp_f32_e32 v16, v16
	v_fmamk_f32 v13, v13, 0x3b808081, v227
	v_fmamk_f32 v14, v14, 0x3b808081, v227
	v_rcp_f32_e32 v13, v13
	v_rcp_f32_e32 v14, v14
	v_fmamk_f32 v15, v15, 0x3b808081, v227
	v_fmamk_f32 v16, v16, 0x3b808081, v227
	v_rcp_f32_e32 v15, v15
	v_rcp_f32_e32 v16, v16
	v_max_f32_e32 v13, 1.0, v13
	v_max_f32_e32 v14, 1.0, v14
	v_cvt_pk_u8_f32 v13, v13, 0, 0
	v_cvt_pk_u8_f32 v14, v14, 0, 0
	v_max_f32_e32 v15, 1.0, v15
	v_max_f32_e32 v16, 1.0, v16
	v_cvt_pk_u8_f32 v13, v15, 1, v13
	v_cvt_pk_u8_f32 v14, v16, 1, v14
	v_mul_f32_e32 v15, v66, v11
	v_mul_f32_e32 v16, v62, v11
	v_exp_f32_e32 v15, v15
	v_exp_f32_e32 v16, v16
	v_lshl_add_u64 v[8:9], v[8:9], 0, v[4:5]
	v_mad_i64_i32 v[6:7], s[20:21], v12, s13, v[6:7]
	v_fmamk_f32 v15, v15, 0x3b808081, v227
	v_fmamk_f32 v16, v16, 0x3b808081, v227
	v_rcp_f32_e32 v15, v15
	v_rcp_f32_e32 v16, v16
	v_lshl_add_u64 v[4:5], v[6:7], 0, v[4:5]
	v_mul_f32_e32 v6, 0x3c000000, v10
	v_max_f32_e32 v15, 1.0, v15
	v_max_f32_e32 v16, 1.0, v16
	v_cvt_pk_u8_f32 v13, v15, 2, v13
	v_cvt_pk_u8_f32 v15, v16, 2, v14
	v_mul_f32_e32 v14, v67, v11
	v_mul_f32_e32 v16, v63, v11
	v_exp_f32_e32 v14, v14
	v_exp_f32_e32 v16, v16
	s_mov_b64 s[20:21], -1
	v_fmamk_f32 v14, v14, 0x3b808081, v227
	v_fmamk_f32 v16, v16, 0x3b808081, v227
	v_rcp_f32_e32 v14, v14
	v_rcp_f32_e32 v16, v16
	v_max_f32_e32 v14, 1.0, v14
	v_max_f32_e32 v16, 1.0, v16
	v_cvt_pk_u8_f32 v14, v14, 3, v13
	v_cvt_pk_u8_f32 v15, v16, 3, v15
	global_store_dwordx2 v[8:9], v[14:15], off
	v_mul_f32_e32 v13, v56, v11
	v_mul_f32_e32 v14, v52, v11
	v_exp_f32_e32 v13, v13
	v_exp_f32_e32 v14, v14
	v_mul_f32_e32 v15, v57, v11
	v_mul_f32_e32 v16, v53, v11
	v_exp_f32_e32 v15, v15
	v_exp_f32_e32 v16, v16
	v_fmamk_f32 v13, v13, 0x3b808081, v227
	v_fmamk_f32 v14, v14, 0x3b808081, v227
	v_rcp_f32_e32 v13, v13
	v_rcp_f32_e32 v14, v14
	v_fmamk_f32 v15, v15, 0x3b808081, v227
	v_fmamk_f32 v16, v16, 0x3b808081, v227
	v_rcp_f32_e32 v15, v15
	v_rcp_f32_e32 v16, v16
	v_max_f32_e32 v13, 1.0, v13
	v_max_f32_e32 v14, 1.0, v14
	v_cvt_pk_u8_f32 v13, v13, 0, 0
	v_cvt_pk_u8_f32 v14, v14, 0, 0
	v_max_f32_e32 v15, 1.0, v15
	v_max_f32_e32 v16, 1.0, v16
	v_cvt_pk_u8_f32 v13, v15, 1, v13
	v_cvt_pk_u8_f32 v14, v16, 1, v14
	v_mul_f32_e32 v15, v58, v11
	v_mul_f32_e32 v16, v54, v11
	v_exp_f32_e32 v15, v15
	v_exp_f32_e32 v16, v16
	v_fmamk_f32 v15, v15, 0x3b808081, v227
	v_fmamk_f32 v16, v16, 0x3b808081, v227
	v_rcp_f32_e32 v15, v15
	v_rcp_f32_e32 v16, v16
	v_max_f32_e32 v15, 1.0, v15
	v_max_f32_e32 v16, 1.0, v16
	v_cvt_pk_u8_f32 v13, v15, 2, v13
	v_cvt_pk_u8_f32 v15, v16, 2, v14
	v_mul_f32_e32 v14, v59, v11
	v_mul_f32_e32 v11, v55, v11
	v_exp_f32_e32 v14, v14
	v_exp_f32_e32 v11, v11
	v_fmamk_f32 v14, v14, 0x3b808081, v227
	v_fmamk_f32 v11, v11, 0x3b808081, v227
	v_rcp_f32_e32 v14, v14
	v_rcp_f32_e32 v11, v11
	v_max_f32_e32 v14, 1.0, v14
	v_max_f32_e32 v11, 1.0, v11
	v_cvt_pk_u8_f32 v14, v14, 3, v13
	v_cvt_pk_u8_f32 v15, v11, 3, v15
	global_store_dwordx2 v[8:9], v[14:15], off offset:128
	v_mul_f32_e32 v8, 0xbfb8aa3b, v6
	v_mul_f32_e32 v6, v48, v8
	v_mul_f32_e32 v7, v44, v8
	v_exp_f32_e32 v6, v6
	v_exp_f32_e32 v7, v7
	v_mul_f32_e32 v9, v49, v8
	v_mul_f32_e32 v10, v45, v8
	v_exp_f32_e32 v9, v9
	v_exp_f32_e32 v10, v10
	v_fmamk_f32 v6, v6, 0x3b808081, v227
	v_fmamk_f32 v7, v7, 0x3b808081, v227
	v_rcp_f32_e32 v6, v6
	v_rcp_f32_e32 v7, v7
	v_fmamk_f32 v9, v9, 0x3b808081, v227
	v_fmamk_f32 v10, v10, 0x3b808081, v227
	v_rcp_f32_e32 v9, v9
	v_rcp_f32_e32 v10, v10
	v_max_f32_e32 v6, 1.0, v6
	v_max_f32_e32 v7, 1.0, v7
	v_cvt_pk_u8_f32 v6, v6, 0, 0
	v_cvt_pk_u8_f32 v7, v7, 0, 0
	v_max_f32_e32 v9, 1.0, v9
	v_max_f32_e32 v10, 1.0, v10
	v_cvt_pk_u8_f32 v6, v9, 1, v6
	v_cvt_pk_u8_f32 v7, v10, 1, v7
	v_mul_f32_e32 v9, v50, v8
	v_mul_f32_e32 v10, v46, v8
	v_exp_f32_e32 v9, v9
	v_exp_f32_e32 v10, v10
	v_fmamk_f32 v9, v9, 0x3b808081, v227
	v_fmamk_f32 v10, v10, 0x3b808081, v227
	v_rcp_f32_e32 v9, v9
	v_rcp_f32_e32 v10, v10
	v_max_f32_e32 v9, 1.0, v9
	v_max_f32_e32 v10, 1.0, v10
	v_cvt_pk_u8_f32 v6, v9, 2, v6
	v_cvt_pk_u8_f32 v7, v10, 2, v7
	v_mul_f32_e32 v9, v51, v8
	v_mul_f32_e32 v10, v47, v8
	v_exp_f32_e32 v9, v9
	v_exp_f32_e32 v10, v10
	v_fmamk_f32 v9, v9, 0x3b808081, v227
	v_fmamk_f32 v10, v10, 0x3b808081, v227
	v_rcp_f32_e32 v9, v9
	v_rcp_f32_e32 v10, v10
	v_max_f32_e32 v9, 1.0, v9
	v_max_f32_e32 v10, 1.0, v10
	v_cvt_pk_u8_f32 v6, v9, 3, v6
	v_cvt_pk_u8_f32 v7, v10, 3, v7
	global_store_dwordx2 v[4:5], v[6:7], off
	v_mul_f32_e32 v6, v40, v8
	v_exp_f32_e32 v6, v6
	v_mul_f32_e32 v9, v41, v8
	v_exp_f32_e32 v9, v9
	v_mul_f32_e32 v7, v36, v8
	v_fmamk_f32 v6, v6, 0x3b808081, v227
	v_rcp_f32_e32 v6, v6
	v_fmamk_f32 v9, v9, 0x3b808081, v227
	v_rcp_f32_e32 v9, v9
	v_exp_f32_e32 v7, v7
	v_max_f32_e32 v6, 1.0, v6
	v_cvt_pk_u8_f32 v6, v6, 0, 0
	v_max_f32_e32 v9, 1.0, v9
	v_mul_f32_e32 v10, v37, v8
	v_exp_f32_e32 v10, v10
	v_cvt_pk_u8_f32 v6, v9, 1, v6
	v_mul_f32_e32 v9, v42, v8
	v_exp_f32_e32 v9, v9
	v_fmamk_f32 v7, v7, 0x3b808081, v227
	v_rcp_f32_e32 v7, v7
	v_fmamk_f32 v10, v10, 0x3b808081, v227
	v_rcp_f32_e32 v10, v10
	v_fmamk_f32 v9, v9, 0x3b808081, v227
	v_rcp_f32_e32 v9, v9
	v_max_f32_e32 v7, 1.0, v7
	v_cvt_pk_u8_f32 v7, v7, 0, 0
	v_max_f32_e32 v10, 1.0, v10
	v_cvt_pk_u8_f32 v7, v10, 1, v7
	v_max_f32_e32 v9, 1.0, v9
	v_mul_f32_e32 v10, v38, v8
	v_exp_f32_e32 v10, v10
	v_cvt_pk_u8_f32 v6, v9, 2, v6
	v_mul_f32_e32 v9, v43, v8
	v_mul_f32_e32 v8, v39, v8
	v_exp_f32_e32 v9, v9
	v_exp_f32_e32 v8, v8
	v_fmamk_f32 v10, v10, 0x3b808081, v227
	v_rcp_f32_e32 v10, v10
	v_fmamk_f32 v9, v9, 0x3b808081, v227
	v_fmamk_f32 v8, v8, 0x3b808081, v227
	v_rcp_f32_e32 v9, v9
	v_rcp_f32_e32 v8, v8
	v_max_f32_e32 v10, 1.0, v10
	v_cvt_pk_u8_f32 v7, v10, 2, v7
	v_max_f32_e32 v9, 1.0, v9
	v_max_f32_e32 v8, 1.0, v8
	v_cvt_pk_u8_f32 v6, v9, 3, v6
	v_cvt_pk_u8_f32 v7, v8, 3, v7
	global_store_dwordx2 v[4:5], v[6:7], off offset:128
	s_cbranch_vccnz .LBB0_167
	s_andn2_b64 vcc, exec, s[0:1]
	s_cbranch_vccnz .LBB0_166
	s_barrier
	s_branch .LBB0_166
.LBB0_181:
	v_mov_b32_e32 v226, 0x44ffe000
	v_mov_b32_e32 v229, 0xff800000
	v_mov_b32_e32 v240, 0x43e00000
	v_mbcnt_lo_u32_b32 v251, -1, 0
	s_waitcnt vmcnt(0)
	s_mov_b32 s72, s62
	s_mov_b32 s25, 0x800000
	s_movk_i32 s24, 0x7200
	s_movk_i32 s20, 0x110
	s_barrier

.LBB0_194:
	v_lshl_add_u32 v146, s18, 8, v151
	v_ashrrev_i32_e32 v147, 31, v146
	v_lshl_add_u64 v[148:149], v[146:147], 2, s[4:5]
	global_load_dword v156, v[148:149], off offset:64
	global_load_dword v152, v[148:149], off offset:128
	global_load_dword v150, v[148:149], off offset:192
	global_load_dword v160, v[148:149], off
	global_load_dword v226, v[148:149], off offset:576
	global_load_dword v227, v[148:149], off offset:640
	global_load_dword v229, v[148:149], off offset:704
	global_load_dword v240, v[148:149], off offset:512
	v_lshl_or_b32 v144, s19, 8, v153
	v_ashrrev_i32_e32 v145, 31, v144
	v_mov_b64_e32 v[142:143], s[6:7]
	s_movk_i32 s24, 0x7200
	v_mad_i64_i32 v[158:159], s[18:19], v146, s24, v[142:143]
	v_lshlrev_b64 v[144:145], 1, v[144:145]
	v_lshl_add_u64 v[158:159], v[158:159], 0, v[144:145]
	s_andn2_b64 vcc, exec, s[36:37]
	s_mov_b32 s25, 0x800000
	s_waitcnt lgkmcnt(0)
	s_waitcnt vmcnt(7)
	v_pk_mul_f32 v[114:115], v[114:115], v[156:157] op_sel_hi:[1,0]
	v_pk_mul_f32 v[106:107], v[106:107], v[156:157] op_sel_hi:[1,0]
	s_waitcnt vmcnt(6)
	v_pk_mul_f32 v[98:99], v[98:99], v[152:153] op_sel_hi:[1,0]
	s_waitcnt vmcnt(4)
	v_pk_mul_f32 v[162:163], v[126:127], v[160:161] op_sel_hi:[1,0]
	v_pk_mul_f32 v[126:127], v[124:125], v[160:161] op_sel_hi:[1,0]
	v_pk_mul_f32 v[130:131], v[130:131], v[160:161] op_sel_hi:[1,0]
	v_pk_mul_f32 v[124:125], v[128:129], v[160:161] op_sel_hi:[1,0]
	v_cvt_pk_bf16_f32 v126, v126, v127
	v_cvt_pk_bf16_f32 v124, v124, v125
	v_cvt_pk_bf16_f32 v125, v130, v131
	v_cvt_pk_bf16_f32 v127, v162, v163
	global_store_dwordx4 v[158:159], v[124:127], off
	v_pk_mul_f32 v[122:123], v[122:123], v[160:161] op_sel_hi:[1,0]
	v_pk_mul_f32 v[90:91], v[90:91], v[152:153] op_sel_hi:[1,0]
	v_pk_mul_f32 v[124:125], v[118:119], v[160:161] op_sel_hi:[1,0]
	v_pk_mul_f32 v[118:119], v[116:117], v[160:161] op_sel_hi:[1,0]
	v_pk_mul_f32 v[116:117], v[120:121], v[160:161] op_sel_hi:[1,0]
	v_cvt_pk_bf16_f32 v118, v118, v119
	v_cvt_pk_bf16_f32 v116, v116, v117
	v_cvt_pk_bf16_f32 v117, v122, v123
	v_cvt_pk_bf16_f32 v119, v124, v125
	global_store_dwordx4 v[158:159], v[116:119], off offset:256
	v_pk_mul_f32 v[82:83], v[82:83], v[150:151] op_sel_hi:[1,0]
	v_pk_mul_f32 v[74:75], v[74:75], v[150:151] op_sel_hi:[1,0]
	v_or_b32_e32 v116, 16, v146
	v_mad_i64_i32 v[116:117], s[18:19], v116, s24, v[142:143]
	v_pk_mul_f32 v[118:119], v[110:111], v[156:157] op_sel_hi:[1,0]
	v_pk_mul_f32 v[110:111], v[108:109], v[156:157] op_sel_hi:[1,0]
	v_pk_mul_f32 v[108:109], v[112:113], v[156:157] op_sel_hi:[1,0]
	v_lshl_add_u64 v[116:117], v[116:117], 0, v[144:145]
	v_cvt_pk_bf16_f32 v108, v108, v109
	v_cvt_pk_bf16_f32 v109, v114, v115
	v_cvt_pk_bf16_f32 v110, v110, v111
	v_cvt_pk_bf16_f32 v111, v118, v119
	global_store_dwordx4 v[116:117], v[108:111], off
	s_nop 1
	v_pk_mul_f32 v[108:109], v[102:103], v[156:157] op_sel_hi:[1,0]
	v_pk_mul_f32 v[102:103], v[100:101], v[156:157] op_sel_hi:[1,0]
	v_pk_mul_f32 v[100:101], v[104:105], v[156:157] op_sel_hi:[1,0]
	v_cvt_pk_bf16_f32 v102, v102, v103
	v_cvt_pk_bf16_f32 v100, v100, v101
	v_cvt_pk_bf16_f32 v101, v106, v107
	v_cvt_pk_bf16_f32 v103, v108, v109
	global_store_dwordx4 v[116:117], v[100:103], off offset:256
	s_nop 1
	v_or_b32_e32 v100, 32, v146
	v_mad_i64_i32 v[100:101], s[18:19], v100, s24, v[142:143]
	v_pk_mul_f32 v[102:103], v[94:95], v[152:153] op_sel_hi:[1,0]
	v_pk_mul_f32 v[94:95], v[92:93], v[152:153] op_sel_hi:[1,0]
	v_pk_mul_f32 v[92:93], v[96:97], v[152:153] op_sel_hi:[1,0]
	v_lshl_add_u64 v[100:101], v[100:101], 0, v[144:145]
	v_cvt_pk_bf16_f32 v92, v92, v93
	v_cvt_pk_bf16_f32 v93, v98, v99
	v_cvt_pk_bf16_f32 v94, v94, v95
	v_cvt_pk_bf16_f32 v95, v102, v103
	global_store_dwordx4 v[100:101], v[92:95], off
	s_nop 1
	v_pk_mul_f32 v[92:93], v[86:87], v[152:153] op_sel_hi:[1,0]
	v_pk_mul_f32 v[86:87], v[84:85], v[152:153] op_sel_hi:[1,0]
	v_pk_mul_f32 v[84:85], v[88:89], v[152:153] op_sel_hi:[1,0]
	v_cvt_pk_bf16_f32 v86, v86, v87
	v_cvt_pk_bf16_f32 v84, v84, v85
	v_cvt_pk_bf16_f32 v85, v90, v91
	v_cvt_pk_bf16_f32 v87, v92, v93
	global_store_dwordx4 v[100:101], v[84:87], off offset:256
	s_nop 1
	v_or_b32_e32 v84, 48, v146
	v_mad_i64_i32 v[84:85], s[18:19], v84, s24, v[142:143]
	v_pk_mul_f32 v[86:87], v[78:79], v[150:151] op_sel_hi:[1,0]
	v_pk_mul_f32 v[78:79], v[76:77], v[150:151] op_sel_hi:[1,0]
	v_pk_mul_f32 v[76:77], v[80:81], v[150:151] op_sel_hi:[1,0]
	v_lshl_add_u64 v[84:85], v[84:85], 0, v[144:145]
	v_cvt_pk_bf16_f32 v76, v76, v77
	v_cvt_pk_bf16_f32 v77, v82, v83
	v_cvt_pk_bf16_f32 v78, v78, v79
	v_cvt_pk_bf16_f32 v79, v86, v87
	global_store_dwordx4 v[84:85], v[76:79], off
	s_nop 1
	v_pk_mul_f32 v[76:77], v[70:71], v[150:151] op_sel_hi:[1,0]
	v_pk_mul_f32 v[70:71], v[68:69], v[150:151] op_sel_hi:[1,0]
	v_pk_mul_f32 v[68:69], v[72:73], v[150:151] op_sel_hi:[1,0]
	v_cvt_pk_bf16_f32 v70, v70, v71
	v_cvt_pk_bf16_f32 v68, v68, v69
	v_cvt_pk_bf16_f32 v69, v74, v75
	v_cvt_pk_bf16_f32 v71, v76, v77
	global_store_dwordx4 v[84:85], v[68:71], off offset:256
	s_waitcnt vmcnt(11)
	v_mov_b32_e32 v72, v226
	s_nop 0
	s_waitcnt vmcnt(10)
	v_mov_b32_e32 v70, v227
	s_waitcnt vmcnt(9)
	v_mov_b32_e32 v68, v229
	s_waitcnt vmcnt(8)
	v_mov_b32_e32 v76, v240
	v_add_u32_e32 v69, 0x80, v146
	v_mad_i64_i32 v[74:75], s[18:19], v69, s24, v[142:143]
	v_lshl_add_u64 v[74:75], v[74:75], 0, v[144:145]
	s_waitcnt lgkmcnt(0)
	v_pk_mul_f32 v[50:51], v[50:51], v[72:73] op_sel_hi:[1,0]
	v_pk_mul_f32 v[42:43], v[42:43], v[72:73] op_sel_hi:[1,0]
	v_pk_mul_f32 v[34:35], v[34:35], v[70:71] op_sel_hi:[1,0]
	v_pk_mul_f32 v[78:79], v[62:63], v[76:77] op_sel_hi:[1,0]
	v_pk_mul_f32 v[62:63], v[60:61], v[76:77] op_sel_hi:[1,0]
	v_pk_mul_f32 v[66:67], v[66:67], v[76:77] op_sel_hi:[1,0]
	v_pk_mul_f32 v[60:61], v[64:65], v[76:77] op_sel_hi:[1,0]
	v_cvt_pk_bf16_f32 v62, v62, v63
	v_cvt_pk_bf16_f32 v60, v60, v61
	v_cvt_pk_bf16_f32 v61, v66, v67
	v_cvt_pk_bf16_f32 v63, v78, v79
	global_store_dwordx4 v[74:75], v[60:63], off
	v_pk_mul_f32 v[58:59], v[58:59], v[76:77] op_sel_hi:[1,0]
	v_pk_mul_f32 v[26:27], v[26:27], v[70:71] op_sel_hi:[1,0]
	v_pk_mul_f32 v[60:61], v[54:55], v[76:77] op_sel_hi:[1,0]
	v_pk_mul_f32 v[54:55], v[52:53], v[76:77] op_sel_hi:[1,0]
	v_pk_mul_f32 v[52:53], v[56:57], v[76:77] op_sel_hi:[1,0]
	v_cvt_pk_bf16_f32 v54, v54, v55
	v_cvt_pk_bf16_f32 v52, v52, v53
	v_cvt_pk_bf16_f32 v53, v58, v59
	v_cvt_pk_bf16_f32 v55, v60, v61
	global_store_dwordx4 v[74:75], v[52:55], off offset:256
	v_pk_mul_f32 v[18:19], v[18:19], v[68:69] op_sel_hi:[1,0]
	v_pk_mul_f32 v[10:11], v[10:11], v[68:69] op_sel_hi:[1,0]
	v_add_u32_e32 v52, 0x90, v146
	v_mad_i64_i32 v[52:53], s[18:19], v52, s24, v[142:143]
	v_pk_mul_f32 v[54:55], v[46:47], v[72:73] op_sel_hi:[1,0]
	v_pk_mul_f32 v[46:47], v[44:45], v[72:73] op_sel_hi:[1,0]
	v_pk_mul_f32 v[44:45], v[48:49], v[72:73] op_sel_hi:[1,0]
	v_lshl_add_u64 v[52:53], v[52:53], 0, v[144:145]
	v_cvt_pk_bf16_f32 v44, v44, v45
	v_cvt_pk_bf16_f32 v45, v50, v51
	v_cvt_pk_bf16_f32 v46, v46, v47
	v_cvt_pk_bf16_f32 v47, v54, v55
	global_store_dwordx4 v[52:53], v[44:47], off
	s_nop 1
	v_pk_mul_f32 v[44:45], v[38:39], v[72:73] op_sel_hi:[1,0]
	v_pk_mul_f32 v[38:39], v[36:37], v[72:73] op_sel_hi:[1,0]
	v_pk_mul_f32 v[36:37], v[40:41], v[72:73] op_sel_hi:[1,0]
	v_cvt_pk_bf16_f32 v38, v38, v39
	v_cvt_pk_bf16_f32 v36, v36, v37
	v_cvt_pk_bf16_f32 v37, v42, v43
	v_cvt_pk_bf16_f32 v39, v44, v45
	global_store_dwordx4 v[52:53], v[36:39], off offset:256
	s_nop 1
	v_add_u32_e32 v36, 0xa0, v146
	v_mad_i64_i32 v[36:37], s[18:19], v36, s24, v[142:143]
	v_pk_mul_f32 v[38:39], v[30:31], v[70:71] op_sel_hi:[1,0]
	v_pk_mul_f32 v[30:31], v[28:29], v[70:71] op_sel_hi:[1,0]
	v_pk_mul_f32 v[28:29], v[32:33], v[70:71] op_sel_hi:[1,0]
	v_lshl_add_u64 v[36:37], v[36:37], 0, v[144:145]
	v_cvt_pk_bf16_f32 v28, v28, v29
	v_cvt_pk_bf16_f32 v29, v34, v35
	v_cvt_pk_bf16_f32 v30, v30, v31
	v_cvt_pk_bf16_f32 v31, v38, v39
	global_store_dwordx4 v[36:37], v[28:31], off
	s_nop 1
	v_pk_mul_f32 v[28:29], v[22:23], v[70:71] op_sel_hi:[1,0]
	v_pk_mul_f32 v[22:23], v[20:21], v[70:71] op_sel_hi:[1,0]
	v_pk_mul_f32 v[20:21], v[24:25], v[70:71] op_sel_hi:[1,0]
	v_cvt_pk_bf16_f32 v22, v22, v23
	v_cvt_pk_bf16_f32 v20, v20, v21
	v_cvt_pk_bf16_f32 v21, v26, v27
	v_cvt_pk_bf16_f32 v23, v28, v29
	global_store_dwordx4 v[36:37], v[20:23], off offset:256
	s_nop 1
	v_add_u32_e32 v20, 0xb0, v146
	v_mad_i64_i32 v[20:21], s[18:19], v20, s24, v[142:143]
	v_pk_mul_f32 v[22:23], v[14:15], v[68:69] op_sel_hi:[1,0]
	v_pk_mul_f32 v[14:15], v[12:13], v[68:69] op_sel_hi:[1,0]
	v_pk_mul_f32 v[12:13], v[16:17], v[68:69] op_sel_hi:[1,0]
	v_lshl_add_u64 v[20:21], v[20:21], 0, v[144:145]
	v_cvt_pk_bf16_f32 v12, v12, v13
	v_cvt_pk_bf16_f32 v13, v18, v19
	v_cvt_pk_bf16_f32 v14, v14, v15
	v_cvt_pk_bf16_f32 v15, v22, v23
	global_store_dwordx4 v[20:21], v[12:15], off
	s_mov_b64 s[18:19], -1
	s_nop 0
	v_pk_mul_f32 v[12:13], v[6:7], v[68:69] op_sel_hi:[1,0]
	v_pk_mul_f32 v[6:7], v[4:5], v[68:69] op_sel_hi:[1,0]
	v_pk_mul_f32 v[4:5], v[8:9], v[68:69] op_sel_hi:[1,0]
	v_cvt_pk_bf16_f32 v6, v6, v7
	v_cvt_pk_bf16_f32 v4, v4, v5
	v_cvt_pk_bf16_f32 v5, v10, v11
	v_cvt_pk_bf16_f32 v7, v12, v13
	global_store_dwordx4 v[20:21], v[4:7], off offset:256
	s_cbranch_vccnz .LBB0_187
	s_andn2_b64 vcc, exec, s[0:1]
	s_cbranch_vccnz .LBB0_186
	s_barrier
	s_branch .LBB0_186
.LBB0_197:
	v_mov_b32_e32 v226, 0x44ffe000
	v_mov_b32_e32 v227, 0x3b808081
	v_mov_b32_e32 v229, 0xff800000
	v_mov_b32_e32 v240, 0x43e00000
	s_waitcnt vmcnt(0)
	s_mov_b32 s72, s62
	s_movk_i32 s20, 0x110
	s_barrier

.LBB0_1841:
	v_lshl_add_u32 v146, s20, 8, v151
	v_ashrrev_i32_e32 v147, 31, v146
	v_lshl_add_u64 v[148:149], v[146:147], 2, s[6:7]
	global_load_dword v156, v[148:149], off offset:64
	global_load_dword v152, v[148:149], off offset:128
	global_load_dword v150, v[148:149], off offset:192
	global_load_dword v160, v[148:149], off
	global_load_dword v226, v[148:149], off offset:576
	global_load_dword v227, v[148:149], off offset:640
	global_load_dword v229, v[148:149], off offset:704
	global_load_dword v240, v[148:149], off offset:512
	v_lshl_or_b32 v144, s21, 8, v154
	v_ashrrev_i32_e32 v145, 31, v144
	v_mov_b64_e32 v[142:143], s[8:9]
	s_movk_i32 s13, 0x2c00
	v_mad_i64_i32 v[158:159], s[20:21], v146, s13, v[142:143]
	v_lshlrev_b64 v[144:145], 1, v[144:145]
	v_lshl_add_u64 v[158:159], v[158:159], 0, v[144:145]
	s_andn2_b64 vcc, exec, s[36:37]
	s_waitcnt lgkmcnt(0)
	s_waitcnt vmcnt(7)
	v_pk_mul_f32 v[114:115], v[114:115], v[156:157] op_sel_hi:[1,0]
	v_pk_mul_f32 v[106:107], v[106:107], v[156:157] op_sel_hi:[1,0]
	s_waitcnt vmcnt(6)
	v_pk_mul_f32 v[98:99], v[98:99], v[152:153] op_sel_hi:[1,0]
	s_waitcnt vmcnt(4)
	v_pk_mul_f32 v[162:163], v[126:127], v[160:161] op_sel_hi:[1,0]
	v_pk_mul_f32 v[126:127], v[124:125], v[160:161] op_sel_hi:[1,0]
	v_pk_mul_f32 v[130:131], v[130:131], v[160:161] op_sel_hi:[1,0]
	v_pk_mul_f32 v[124:125], v[128:129], v[160:161] op_sel_hi:[1,0]
	v_cvt_pk_bf16_f32 v126, v126, v127
	v_cvt_pk_bf16_f32 v124, v124, v125
	v_cvt_pk_bf16_f32 v125, v130, v131
	v_cvt_pk_bf16_f32 v127, v162, v163
	global_store_dwordx4 v[158:159], v[124:127], off
	v_pk_mul_f32 v[122:123], v[122:123], v[160:161] op_sel_hi:[1,0]
	v_pk_mul_f32 v[90:91], v[90:91], v[152:153] op_sel_hi:[1,0]
	v_pk_mul_f32 v[124:125], v[118:119], v[160:161] op_sel_hi:[1,0]
	v_pk_mul_f32 v[118:119], v[116:117], v[160:161] op_sel_hi:[1,0]
	v_pk_mul_f32 v[116:117], v[120:121], v[160:161] op_sel_hi:[1,0]
	v_cvt_pk_bf16_f32 v118, v118, v119
	v_cvt_pk_bf16_f32 v116, v116, v117
	v_cvt_pk_bf16_f32 v117, v122, v123
	v_cvt_pk_bf16_f32 v119, v124, v125
	global_store_dwordx4 v[158:159], v[116:119], off offset:256
	v_pk_mul_f32 v[82:83], v[82:83], v[150:151] op_sel_hi:[1,0]
	v_pk_mul_f32 v[74:75], v[74:75], v[150:151] op_sel_hi:[1,0]
	v_or_b32_e32 v116, 16, v146
	v_mad_i64_i32 v[116:117], s[20:21], v116, s13, v[142:143]
	v_pk_mul_f32 v[118:119], v[110:111], v[156:157] op_sel_hi:[1,0]
	v_pk_mul_f32 v[110:111], v[108:109], v[156:157] op_sel_hi:[1,0]
	v_pk_mul_f32 v[108:109], v[112:113], v[156:157] op_sel_hi:[1,0]
	v_lshl_add_u64 v[116:117], v[116:117], 0, v[144:145]
	v_cvt_pk_bf16_f32 v108, v108, v109
	v_cvt_pk_bf16_f32 v109, v114, v115
	v_cvt_pk_bf16_f32 v110, v110, v111
	v_cvt_pk_bf16_f32 v111, v118, v119
	global_store_dwordx4 v[116:117], v[108:111], off
	s_nop 1
	v_pk_mul_f32 v[108:109], v[102:103], v[156:157] op_sel_hi:[1,0]
	v_pk_mul_f32 v[102:103], v[100:101], v[156:157] op_sel_hi:[1,0]
	v_pk_mul_f32 v[100:101], v[104:105], v[156:157] op_sel_hi:[1,0]
	v_cvt_pk_bf16_f32 v102, v102, v103
	v_cvt_pk_bf16_f32 v100, v100, v101
	v_cvt_pk_bf16_f32 v101, v106, v107
	v_cvt_pk_bf16_f32 v103, v108, v109
	global_store_dwordx4 v[116:117], v[100:103], off offset:256
	s_nop 1
	v_or_b32_e32 v100, 32, v146
	v_mad_i64_i32 v[100:101], s[20:21], v100, s13, v[142:143]
	v_pk_mul_f32 v[102:103], v[94:95], v[152:153] op_sel_hi:[1,0]
	v_pk_mul_f32 v[94:95], v[92:93], v[152:153] op_sel_hi:[1,0]
	v_pk_mul_f32 v[92:93], v[96:97], v[152:153] op_sel_hi:[1,0]
	v_lshl_add_u64 v[100:101], v[100:101], 0, v[144:145]
	v_cvt_pk_bf16_f32 v92, v92, v93
	v_cvt_pk_bf16_f32 v93, v98, v99
	v_cvt_pk_bf16_f32 v94, v94, v95
	v_cvt_pk_bf16_f32 v95, v102, v103
	global_store_dwordx4 v[100:101], v[92:95], off
	s_nop 1
	v_pk_mul_f32 v[92:93], v[86:87], v[152:153] op_sel_hi:[1,0]
	v_pk_mul_f32 v[86:87], v[84:85], v[152:153] op_sel_hi:[1,0]
	v_pk_mul_f32 v[84:85], v[88:89], v[152:153] op_sel_hi:[1,0]
	v_cvt_pk_bf16_f32 v86, v86, v87
	v_cvt_pk_bf16_f32 v84, v84, v85
	v_cvt_pk_bf16_f32 v85, v90, v91
	v_cvt_pk_bf16_f32 v87, v92, v93
	global_store_dwordx4 v[100:101], v[84:87], off offset:256
	s_nop 1
	v_or_b32_e32 v84, 48, v146
	v_mad_i64_i32 v[84:85], s[20:21], v84, s13, v[142:143]
	v_pk_mul_f32 v[86:87], v[78:79], v[150:151] op_sel_hi:[1,0]
	v_pk_mul_f32 v[78:79], v[76:77], v[150:151] op_sel_hi:[1,0]
	v_pk_mul_f32 v[76:77], v[80:81], v[150:151] op_sel_hi:[1,0]
	v_lshl_add_u64 v[84:85], v[84:85], 0, v[144:145]
	v_cvt_pk_bf16_f32 v76, v76, v77
	v_cvt_pk_bf16_f32 v77, v82, v83
	v_cvt_pk_bf16_f32 v78, v78, v79
	v_cvt_pk_bf16_f32 v79, v86, v87
	global_store_dwordx4 v[84:85], v[76:79], off
	s_nop 1
	v_pk_mul_f32 v[76:77], v[70:71], v[150:151] op_sel_hi:[1,0]
	v_pk_mul_f32 v[70:71], v[68:69], v[150:151] op_sel_hi:[1,0]
	v_pk_mul_f32 v[68:69], v[72:73], v[150:151] op_sel_hi:[1,0]
	v_cvt_pk_bf16_f32 v70, v70, v71
	v_cvt_pk_bf16_f32 v68, v68, v69
	v_cvt_pk_bf16_f32 v69, v74, v75
	v_cvt_pk_bf16_f32 v71, v76, v77
	global_store_dwordx4 v[84:85], v[68:71], off offset:256
	s_waitcnt vmcnt(11)
	v_mov_b32_e32 v72, v226
	s_nop 0
	s_waitcnt vmcnt(10)
	v_mov_b32_e32 v70, v227
	s_waitcnt vmcnt(9)
	v_mov_b32_e32 v68, v229
	s_waitcnt vmcnt(8)
	v_mov_b32_e32 v76, v240
	v_add_u32_e32 v69, 0x80, v146
	v_mad_i64_i32 v[74:75], s[20:21], v69, s13, v[142:143]
	v_lshl_add_u64 v[74:75], v[74:75], 0, v[144:145]
	s_waitcnt lgkmcnt(0)
	v_pk_mul_f32 v[50:51], v[50:51], v[72:73] op_sel_hi:[1,0]
	v_pk_mul_f32 v[42:43], v[42:43], v[72:73] op_sel_hi:[1,0]
	v_pk_mul_f32 v[34:35], v[34:35], v[70:71] op_sel_hi:[1,0]
	v_pk_mul_f32 v[78:79], v[62:63], v[76:77] op_sel_hi:[1,0]
	v_pk_mul_f32 v[62:63], v[60:61], v[76:77] op_sel_hi:[1,0]
	v_pk_mul_f32 v[66:67], v[66:67], v[76:77] op_sel_hi:[1,0]
	v_pk_mul_f32 v[60:61], v[64:65], v[76:77] op_sel_hi:[1,0]
	v_cvt_pk_bf16_f32 v62, v62, v63
	v_cvt_pk_bf16_f32 v60, v60, v61
	v_cvt_pk_bf16_f32 v61, v66, v67
	v_cvt_pk_bf16_f32 v63, v78, v79
	global_store_dwordx4 v[74:75], v[60:63], off
	v_pk_mul_f32 v[58:59], v[58:59], v[76:77] op_sel_hi:[1,0]
	v_pk_mul_f32 v[26:27], v[26:27], v[70:71] op_sel_hi:[1,0]
	v_pk_mul_f32 v[60:61], v[54:55], v[76:77] op_sel_hi:[1,0]
	v_pk_mul_f32 v[54:55], v[52:53], v[76:77] op_sel_hi:[1,0]
	v_pk_mul_f32 v[52:53], v[56:57], v[76:77] op_sel_hi:[1,0]
	v_cvt_pk_bf16_f32 v54, v54, v55
	v_cvt_pk_bf16_f32 v52, v52, v53
	v_cvt_pk_bf16_f32 v53, v58, v59
	v_cvt_pk_bf16_f32 v55, v60, v61
	global_store_dwordx4 v[74:75], v[52:55], off offset:256
	v_pk_mul_f32 v[18:19], v[18:19], v[68:69] op_sel_hi:[1,0]
	v_pk_mul_f32 v[10:11], v[10:11], v[68:69] op_sel_hi:[1,0]
	v_add_u32_e32 v52, 0x90, v146
	v_mad_i64_i32 v[52:53], s[20:21], v52, s13, v[142:143]
	v_pk_mul_f32 v[54:55], v[46:47], v[72:73] op_sel_hi:[1,0]
	v_pk_mul_f32 v[46:47], v[44:45], v[72:73] op_sel_hi:[1,0]
	v_pk_mul_f32 v[44:45], v[48:49], v[72:73] op_sel_hi:[1,0]
	v_lshl_add_u64 v[52:53], v[52:53], 0, v[144:145]
	v_cvt_pk_bf16_f32 v44, v44, v45
	v_cvt_pk_bf16_f32 v45, v50, v51
	v_cvt_pk_bf16_f32 v46, v46, v47
	v_cvt_pk_bf16_f32 v47, v54, v55
	global_store_dwordx4 v[52:53], v[44:47], off
	s_nop 1
	v_pk_mul_f32 v[44:45], v[38:39], v[72:73] op_sel_hi:[1,0]
	v_pk_mul_f32 v[38:39], v[36:37], v[72:73] op_sel_hi:[1,0]
	v_pk_mul_f32 v[36:37], v[40:41], v[72:73] op_sel_hi:[1,0]
	v_cvt_pk_bf16_f32 v38, v38, v39
	v_cvt_pk_bf16_f32 v36, v36, v37
	v_cvt_pk_bf16_f32 v37, v42, v43
	v_cvt_pk_bf16_f32 v39, v44, v45
	global_store_dwordx4 v[52:53], v[36:39], off offset:256
	s_nop 1
	v_add_u32_e32 v36, 0xa0, v146
	v_mad_i64_i32 v[36:37], s[20:21], v36, s13, v[142:143]
	v_pk_mul_f32 v[38:39], v[30:31], v[70:71] op_sel_hi:[1,0]
	v_pk_mul_f32 v[30:31], v[28:29], v[70:71] op_sel_hi:[1,0]
	v_pk_mul_f32 v[28:29], v[32:33], v[70:71] op_sel_hi:[1,0]
	v_lshl_add_u64 v[36:37], v[36:37], 0, v[144:145]
	v_cvt_pk_bf16_f32 v28, v28, v29
	v_cvt_pk_bf16_f32 v29, v34, v35
	v_cvt_pk_bf16_f32 v30, v30, v31
	v_cvt_pk_bf16_f32 v31, v38, v39
	global_store_dwordx4 v[36:37], v[28:31], off
	s_nop 1
	v_pk_mul_f32 v[28:29], v[22:23], v[70:71] op_sel_hi:[1,0]
	v_pk_mul_f32 v[22:23], v[20:21], v[70:71] op_sel_hi:[1,0]
	v_pk_mul_f32 v[20:21], v[24:25], v[70:71] op_sel_hi:[1,0]
	v_cvt_pk_bf16_f32 v22, v22, v23
	v_cvt_pk_bf16_f32 v20, v20, v21
	v_cvt_pk_bf16_f32 v21, v26, v27
	v_cvt_pk_bf16_f32 v23, v28, v29
	global_store_dwordx4 v[36:37], v[20:23], off offset:256
	s_nop 1
	v_add_u32_e32 v20, 0xb0, v146
	v_mad_i64_i32 v[20:21], s[20:21], v20, s13, v[142:143]
	v_pk_mul_f32 v[22:23], v[14:15], v[68:69] op_sel_hi:[1,0]
	v_pk_mul_f32 v[14:15], v[12:13], v[68:69] op_sel_hi:[1,0]
	v_pk_mul_f32 v[12:13], v[16:17], v[68:69] op_sel_hi:[1,0]
	v_lshl_add_u64 v[20:21], v[20:21], 0, v[144:145]
	v_cvt_pk_bf16_f32 v12, v12, v13
	v_cvt_pk_bf16_f32 v13, v18, v19
	v_cvt_pk_bf16_f32 v14, v14, v15
	v_cvt_pk_bf16_f32 v15, v22, v23
	global_store_dwordx4 v[20:21], v[12:15], off
	s_mov_b64 s[20:21], -1
	s_nop 0
	v_pk_mul_f32 v[12:13], v[6:7], v[68:69] op_sel_hi:[1,0]
	v_pk_mul_f32 v[6:7], v[4:5], v[68:69] op_sel_hi:[1,0]
	v_pk_mul_f32 v[4:5], v[8:9], v[68:69] op_sel_hi:[1,0]
	v_cvt_pk_bf16_f32 v6, v6, v7
	v_cvt_pk_bf16_f32 v4, v4, v5
	v_cvt_pk_bf16_f32 v5, v10, v11
	v_cvt_pk_bf16_f32 v7, v12, v13
	global_store_dwordx4 v[20:21], v[4:7], off offset:256
	s_cbranch_vccnz .LBB0_1834
	s_andn2_b64 vcc, exec, s[0:1]
	s_cbranch_vccnz .LBB0_1833
	s_barrier
	s_branch .LBB0_1833
.LBB0_1844:
	v_mov_b32_e32 v226, 0x44ffe000
	v_mov_b32_e32 v227, 0x3b808081
	v_mov_b32_e32 v229, 0xff800000
	v_mov_b32_e32 v240, 0x43e00000
	s_waitcnt vmcnt(0)
	s_mov_b32 s72, s64
	s_mov_b32 s25, 0x800000
	s_movk_i32 s24, 0x7200
	s_movk_i32 s20, 0x110
	s_barrier
